# P6 reuses the expert tables left in LDS by the gate_up phase (no expert-count reload, no second row-prefix pass)
# baseline (speedup 1.0000x reference)
; #define LAS3 __attribute__((address_space(3)))
; __device__ __forceinline__ int lane_id() { int r; asm volatile("v_mbcnt_lo_u32_b32 %0, -1, 0\n\tv_mbcnt_hi_u32_b32 %0, -1, %0" : "=v"(r)); return r; }
; template <int EPI>
; __device__ __forceinline__ int* moe_phase(const Params& p, LAS3 char* lds, int wid, int* pend_in) {
;     ...
;     LAS3 int* xcnt = (LAS3 int*)(lds + LDS_MISC + 1024);
;     { const int t0 = wid * 64 + lane_id(); if (t0 < NE) { const int c = p.cnt[t0]; mtv[t0] = (c + 255) >> 8; xcnt[t0] = c; } }
;     __syncthreads();
;     { const int t0 = wid * 64 + lane_id(); if (t0 == 8) { int a = 0, b = 0; for (int i = 0; i < NE; ++i) { const int c = xcnt[i]; xcnt[32 + i] = a; xcnt[64 + i] = b; a += c; b += 256 * ((c + 255) >> 8); } } }
.LBB0_510:
	s_or_b64 exec, exec, s[0:1]
	s_waitcnt lgkmcnt(0)
	s_barrier
	v_mbcnt_lo_u32_b32 v0, -1, 0
	v_mbcnt_hi_u32_b32 v0, -1, v0
	s_nop 0
	v_add_u32_e32 v0, s75, v0
	v_cmp_gt_i32_e32 vcc, 32, v0
	s_and_saveexec_b64 s[0:1], vcc
	s_branch .LBB0_512
	v_readlane_b32 s8, v254, 2
	v_ashrrev_i32_e32 v1, 31, v0
	v_readlane_b32 s18, v254, 12
	v_readlane_b32 s19, v254, 13
	v_readlane_b32 s9, v254, 3
	v_readlane_b32 s10, v254, 4
	v_lshl_add_u64 v[2:3], v[0:1], 2, s[18:19]
	global_load_dword v1, v[2:3], off
	v_lshl_add_u32 v0, v0, 2, 0
	v_add_u32_e32 v2, 0x21300, v0
	v_readlane_b32 s11, v254, 5
	v_readlane_b32 s12, v254, 6
	v_readlane_b32 s13, v254, 7
	v_readlane_b32 s14, v254, 8
	v_readlane_b32 s15, v254, 9
	v_readlane_b32 s16, v254, 10
	v_readlane_b32 s17, v254, 11
	v_readlane_b32 s20, v254, 14
	v_readlane_b32 s21, v254, 15
	v_readlane_b32 s22, v254, 16
	v_readlane_b32 s23, v254, 17
	v_add_u32_e32 v0, 0x21400, v0
	s_waitcnt vmcnt(0)
	v_add_u32_e32 v3, 0xff, v1
	v_ashrrev_i32_e32 v3, 8, v3
	ds_write_b32 v2, v3
	ds_write_b32 v0, v1
.LBB0_512:
	s_or_b64 exec, exec, s[0:1]
	s_waitcnt lgkmcnt(0)
	s_barrier
	v_mbcnt_lo_u32_b32 v0, -1, 0
	v_mbcnt_hi_u32_b32 v0, -1, v0
	s_nop 0
	v_add_u32_e32 v0, s75, v0
	v_cmp_eq_u32_e32 vcc, 8, v0
	s_and_saveexec_b64 s[0:1], vcc
	s_branch .LBB0_514
	s_add_i32 s2, 0, 0x21400
	v_mov_b32_e32 v0, s2
	ds_read_b128 v[0:3], v0
	s_add_i32 s2, 0, 0x21410
	s_waitcnt vmcnt(14)
	v_mov_b32_e32 v4, s2
	ds_read_b128 v[4:7], v4
	s_add_i32 s2, 0, 0x21480
	s_waitcnt vmcnt(13) lgkmcnt(1)
	v_add_u32_e32 v8, 0xff, v0
	v_add_u32_e32 v10, v1, v0
	v_add_u32_e32 v1, 0xff, v1
	s_waitcnt vmcnt(12)
	v_and_b32_e32 v13, 0xffffff00, v8
	v_and_b32_e32 v1, 0xffffff00, v1
	v_add_u32_e32 v14, v1, v13
	v_add_u32_e32 v1, 0xff, v2
	v_and_b32_e32 v1, 0xffffff00, v1
	v_add_u32_e32 v11, v2, v10
	v_add_u32_e32 v15, v1, v14
	v_mov_b32_e32 v8, 0
	v_mov_b32_e32 v9, v0
	v_mov_b32_e32 v0, s2
	s_add_i32 s2, 0, 0x21500
	v_add_u32_e32 v1, 0xff, v3
	ds_write_b128 v0, v[8:11]
	v_mov_b32_e32 v12, v8
	v_mov_b32_e32 v0, s2
	v_and_b32_e32 v1, 0xffffff00, v1
	s_waitcnt lgkmcnt(1)
	v_add_u32_e32 v2, 0xff, v4
	ds_write_b128 v0, v[12:15]
	v_add_u32_e32 v0, v3, v11
	v_add_u32_e32 v8, v1, v15
	v_and_b32_e32 v2, 0xffffff00, v2
	v_add_u32_e32 v3, 0xff, v5
	v_add_u32_e32 v1, v4, v0
	v_add_u32_e32 v9, v2, v8
	v_and_b32_e32 v3, 0xffffff00, v3
	v_add_u32_e32 v4, 0xff, v6
	v_add_u32_e32 v2, v5, v1
	v_add_u32_e32 v10, v3, v9
	v_and_b32_e32 v4, 0xffffff00, v4
	s_add_i32 s2, 0, 0x21490
	v_add_u32_e32 v3, v6, v2
	v_add_u32_e32 v11, v4, v10
	v_mov_b32_e32 v4, s2
	s_add_i32 s2, 0, 0x21510
	ds_write_b128 v4, v[0:3]
	v_mov_b32_e32 v0, s2
	s_add_i32 s2, 0, 0x21420
	v_mov_b32_e32 v2, s2
	ds_write_b128 v0, v[8:11]
	v_add_u32_e32 v0, v7, v3
	ds_read_b128 v[2:5], v2
	v_add_u32_e32 v1, 0xff, v7
	v_and_b32_e32 v1, 0xffffff00, v1
	s_add_i32 s2, 0, 0x21430
	v_add_u32_e32 v6, v1, v11
	v_mov_b32_e32 v1, s2
	ds_read_b128 v[10:13], v1
	s_waitcnt lgkmcnt(1)
	v_add_u32_e32 v1, v2, v0
	v_add_u32_e32 v2, 0xff, v2
	v_and_b32_e32 v2, 0xffffff00, v2
	v_add_u32_e32 v7, v2, v6
	v_add_u32_e32 v2, v3, v1
	v_add_u32_e32 v3, 0xff, v3
	v_and_b32_e32 v3, 0xffffff00, v3
	v_add_u32_e32 v8, v3, v7
	v_add_u32_e32 v3, v4, v2
	v_add_u32_e32 v4, 0xff, v4
	v_and_b32_e32 v4, 0xffffff00, v4
	s_add_i32 s2, 0, 0x214a0
	v_add_u32_e32 v9, v4, v8
	v_mov_b32_e32 v4, s2
	s_add_i32 s2, 0, 0x21520
	ds_write_b128 v4, v[0:3]
	v_mov_b32_e32 v0, s2
	v_add_u32_e32 v1, 0xff, v5
	ds_write_b128 v0, v[6:9]
	v_add_u32_e32 v0, v5, v3
	v_and_b32_e32 v1, 0xffffff00, v1
	s_waitcnt lgkmcnt(2)
	v_add_u32_e32 v2, 0xff, v10
	v_add_u32_e32 v4, v1, v9
	v_add_u32_e32 v1, v10, v0
	v_and_b32_e32 v2, 0xffffff00, v2
	v_add_u32_e32 v3, 0xff, v11
	v_add_u32_e32 v5, v2, v4
	v_add_u32_e32 v2, v11, v1
	v_and_b32_e32 v3, 0xffffff00, v3
	s_add_i32 s2, 0, 0x214b0
	v_add_u32_e32 v6, v3, v5
	v_add_u32_e32 v3, v12, v2
	v_add_u32_e32 v7, 0xff, v12
	v_mov_b32_e32 v8, s2
	s_add_i32 s2, 0, 0x21530
	v_and_b32_e32 v7, 0xffffff00, v7
	ds_write_b128 v8, v[0:3]
	v_mov_b32_e32 v0, s2
	s_add_i32 s2, 0, 0x21440
	v_add_u32_e32 v7, v7, v6
	v_mov_b32_e32 v2, s2
	ds_write_b128 v0, v[4:7]
	v_add_u32_e32 v0, v13, v3
	ds_read_b128 v[2:5], v2
	v_add_u32_e32 v1, 0xff, v13
	v_and_b32_e32 v1, 0xffffff00, v1
	s_add_i32 s2, 0, 0x21450
	v_add_u32_e32 v6, v1, v7
	v_mov_b32_e32 v1, s2
	ds_read_b128 v[10:13], v1
	s_waitcnt lgkmcnt(1)
	v_add_u32_e32 v1, v2, v0
	v_add_u32_e32 v2, 0xff, v2
	v_and_b32_e32 v2, 0xffffff00, v2
	v_add_u32_e32 v7, v2, v6
	v_add_u32_e32 v2, v3, v1
	v_add_u32_e32 v3, 0xff, v3
	v_and_b32_e32 v3, 0xffffff00, v3
	v_add_u32_e32 v8, v3, v7
	v_add_u32_e32 v3, v4, v2
	v_add_u32_e32 v4, 0xff, v4
	v_and_b32_e32 v4, 0xffffff00, v4
	s_add_i32 s2, 0, 0x214c0
	v_add_u32_e32 v9, v4, v8
	v_mov_b32_e32 v4, s2
	s_add_i32 s2, 0, 0x21540
	ds_write_b128 v4, v[0:3]
	v_mov_b32_e32 v0, s2
	v_add_u32_e32 v1, 0xff, v5
	ds_write_b128 v0, v[6:9]
	v_add_u32_e32 v0, v5, v3
	v_and_b32_e32 v1, 0xffffff00, v1
	s_waitcnt lgkmcnt(2)
	v_add_u32_e32 v2, 0xff, v10
	v_add_u32_e32 v4, v1, v9
	v_add_u32_e32 v1, v10, v0
	v_and_b32_e32 v2, 0xffffff00, v2
	v_add_u32_e32 v3, 0xff, v11
	v_add_u32_e32 v5, v2, v4
	v_add_u32_e32 v2, v11, v1
	v_and_b32_e32 v3, 0xffffff00, v3
	s_add_i32 s2, 0, 0x214d0
	v_add_u32_e32 v6, v3, v5
	v_add_u32_e32 v3, v12, v2
	v_add_u32_e32 v7, 0xff, v12
	v_mov_b32_e32 v8, s2
	s_add_i32 s2, 0, 0x21550
	v_and_b32_e32 v7, 0xffffff00, v7
	ds_write_b128 v8, v[0:3]
	v_mov_b32_e32 v0, s2
	s_add_i32 s2, 0, 0x21460
	v_add_u32_e32 v7, v7, v6
	v_mov_b32_e32 v2, s2
	ds_write_b128 v0, v[4:7]
	v_add_u32_e32 v0, v13, v3
	ds_read_b128 v[2:5], v2
	v_add_u32_e32 v1, 0xff, v13
	v_and_b32_e32 v1, 0xffffff00, v1
	s_add_i32 s2, 0, 0x21470
	v_add_u32_e32 v6, v1, v7
	v_mov_b32_e32 v1, s2
	ds_read_b96 v[10:12], v1
	s_waitcnt lgkmcnt(1)
	v_add_u32_e32 v1, v2, v0
	v_add_u32_e32 v2, 0xff, v2
	v_and_b32_e32 v2, 0xffffff00, v2
	v_add_u32_e32 v7, v2, v6
	v_add_u32_e32 v2, v3, v1
	v_add_u32_e32 v3, 0xff, v3
	v_and_b32_e32 v3, 0xffffff00, v3
	v_add_u32_e32 v8, v3, v7
	v_add_u32_e32 v3, v4, v2
	v_add_u32_e32 v4, 0xff, v4
	v_and_b32_e32 v4, 0xffffff00, v4
	s_add_i32 s2, 0, 0x214e0
	v_add_u32_e32 v9, v4, v8
	v_mov_b32_e32 v4, s2
	s_add_i32 s2, 0, 0x21560
	ds_write_b128 v4, v[0:3]
	v_mov_b32_e32 v0, s2
	v_add_u32_e32 v1, 0xff, v5
	ds_write_b128 v0, v[6:9]
	v_add_u32_e32 v0, v5, v3
	v_and_b32_e32 v1, 0xffffff00, v1
	s_waitcnt lgkmcnt(2)
	v_add_u32_e32 v2, 0xff, v10
	v_add_u32_e32 v4, v1, v9
	v_add_u32_e32 v1, v10, v0
	v_and_b32_e32 v2, 0xffffff00, v2
	v_add_u32_e32 v3, 0xff, v11
	v_add_u32_e32 v5, v2, v4
	v_add_u32_e32 v2, v11, v1
	v_and_b32_e32 v3, 0xffffff00, v3
	v_add_u32_e32 v7, 0xff, v12
	s_add_i32 s2, 0, 0x214f0
	v_add_u32_e32 v6, v3, v5
	v_add_u32_e32 v3, v12, v2
	v_and_b32_e32 v7, 0xffffff00, v7
	v_mov_b32_e32 v8, s2
	s_add_i32 s2, 0, 0x21570
	v_add_u32_e32 v7, v7, v6
	ds_write_b128 v8, v[0:3]
	v_mov_b32_e32 v0, s2
	ds_write_b128 v0, v[4:7]
